# speedup vs baseline: 1.0259x; 1.0153x over previous
.LBB0_4:
	s_load_dwordx2 s[2:3], s[0:1], 0x0
	s_load_dwordx2 s[0:1], s[0:1], 0x10
	v_and_b32_e32 v3, 7, v2
	v_bfe_u32 v4, v2, 3, 8
	v_bfe_u32 v5, v2, 11, 4
	v_bfe_u32 v6, v2, 15, 2
	v_lshrrev_b32_e32 v7, 17, v2
	v_lshrrev_b32_e32 v8, 7, v4
	v_lshl_or_b32 v8, v6, 1, v8
	v_and_b32_e32 v9, 0x7f, v4
	v_lshrrev_b32_e32 v10, 1, v5
	v_and_b32_e32 v11, 1, v5
	v_lshlrev_b32_e32 v3, 3, v3
	v_lshl_or_b32 v11, v11, 6, v3
	v_lshl_or_b32 v8, v8, 1, v7
	v_lshl_or_b32 v10, v10, 1, v7
	v_lshl_or_b32 v8, v8, 4, v10
	v_lshl_or_b32 v8, v8, 7, v9
	v_lshl_or_b32 v8, v8, 7, v11
	v_lshlrev_b32_e32 v12, 2, v8
	v_lshlrev_b32_e32 v0, 4, v2
	s_waitcnt lgkmcnt(0)
	global_load_dwordx4 v[4:7], v12, s[2:3] nt
	global_load_dwordx4 v[8:11], v12, s[2:3] offset:16 nt
	s_waitcnt vmcnt(1)
	v_cvt_pk_bf16_f32 v4, v4, v5
	v_cvt_pk_bf16_f32 v5, v6, v7
	s_waitcnt vmcnt(0)
	v_cvt_pk_bf16_f32 v6, v8, v9
	v_cvt_pk_bf16_f32 v7, v10, v11
	global_store_dwordx4 v0, v[4:7], s[0:1]
	s_endpgm
